# instruction selection: SB cumsum C-operand broadcast with v_mov_b64 (15 moves -> 8 per tile)
# baseline (speedup 1.0000x reference)
; __device__ __forceinline__ unsigned cvt_pk_bf16(float lo, float hi) { unsigned r; asm volatile("v_cvt_pk_bf16_f32 %0, %1, %2" : "=v"(r) : "v"(lo), "v"(hi)); return r; }
; __device__ __forceinline__ float ex2(float x) { return __builtin_amdgcn_exp2f(x); }
; __device__ __forceinline__ float lg2(float x) { return __builtin_amdgcn_logf(x); }
; __device__ __forceinline__ f32x16 mfma32(bf16x8 a, bf16x8 b, f32x16 c) { return __builtin_amdgcn_mfma_f32_32x32x16_bf16(a, b, c, 0, 0, 0); }
; __device__ __forceinline__ void sb_unit(int b, int h, int qb, const bf16_t* __restrict__ PROJ, bf16_t* OCAT, float* SSQO, ldsp shm, volatile LAS unsigned* FL) {
;     ...
;             for (int r = 0; r < 16; ++r) { l0[r] = -lg2(1.0f + ex2(fminf(z0[r], 100.f))); l1[r] = -lg2(1.0f + ex2(fminf(z1[r], 100.f))); }
;             if (diag) {
; #pragma unroll
;                 for (int r = 0; r < 16; ++r) { const int kk = kb0 + (r & 3) + 8 * (r >> 2); if (kk >= qabs) l0[r] = 0.f; if (kk + 32 >= qabs) l1[r] = 0.f; } }
; #pragma unroll
;             for (int r = 0; r < 16; ++r) { tot += l0[r] + l1[r]; z0[r] += l0[r]; z1[r] += l1[r]; }
;             u32x4 lh[4];
; #pragma unroll
;             for (int k = 0; k < 4; ++k)
; #pragma unroll
;                 for (int j = 0; j < 4; ++j) { const float a = (k < 2) ? l0[(k & 1) * 8 + 2 * j] : l1[(k & 1) * 8 + 2 * j], c = (k < 2) ? l0[(k & 1) * 8 + 2 * j + 1] : l1[(k & 1) * 8 + 2 * j + 1];
;                     lh[k][j] = cvt_pk_bf16(a, c); }
;     ...
;             f32x16 x0, x1;
; #pragma unroll
;             for (int r = 0; r < 16; ++r) { x0[r] = Lc; x1[r] = Lc; }
;             x0 = mfma32(Ta, SB_B(lh[0]), x0); x0 = mfma32(Tb, SB_B(lh[1]), x0); x0 = mfma32(Ton, SB_B(lh[2]), x0); x0 = mfma32(Ton, SB_B(lh[3]), x0);
;             x1 = mfma32(Ta, SB_B(lh[2]), x1); x1 = mfma32(Tb, SB_B(lh[3]), x1);
;     ...
; #pragma unroll
;             for (int r = 0; r < 16; ++r) { z0[r] = ex2(z0[r] + x0[r]); z1[r] = ex2(z1[r] + x1[r]); }
.LBB0_1058:
	v_mov_b32_e32 v37, v36
	v_mov_b64_e32 v[38:39], v[36:37]
	v_mov_b64_e32 v[40:41], v[36:37]
	v_mov_b64_e32 v[42:43], v[36:37]
	v_mov_b64_e32 v[44:45], v[36:37]
	v_mov_b64_e32 v[46:47], v[36:37]
	v_mov_b64_e32 v[48:49], v[36:37]
	v_mov_b64_e32 v[50:51], v[36:37]
	v_cvt_pk_bf16_f32 v200, v2, v1
	v_cvt_pk_bf16_f32 v201, v54, v55
	v_cvt_pk_bf16_f32 v202, v58, v59
	v_cvt_pk_bf16_f32 v203, v62, v63
	v_readlane_b32 s4, v254, 39
	s_nop 0
	v_mfma_f32_32x32x16_bf16 v[114:129], v[150:153], v[200:203], v[36:51]
	v_cvt_pk_bf16_f32 v200, v66, v67
	v_cvt_pk_bf16_f32 v201, v70, v71
	v_cvt_pk_bf16_f32 v202, v74, v75
	v_cvt_pk_bf16_f32 v203, v78, v79
	v_readlane_b32 s6, v254, 41
	v_readlane_b32 s7, v254, 42
	v_readlane_b32 s5, v254, 40
	v_mfma_f32_32x32x16_bf16 v[114:129], v[146:149], v[200:203], v[114:129]
	s_mov_b32 s6, s4
	s_mov_b32 s7, s4
	s_mov_b32 s5, s4
	v_mov_b64_e32 v[206:207], s[6:7]
	v_mov_b64_e32 v[204:205], s[4:5]
	v_cvt_pk_bf16_f32 v200, v52, v53
	v_cvt_pk_bf16_f32 v201, v56, v57
	v_cvt_pk_bf16_f32 v202, v60, v61
	v_cvt_pk_bf16_f32 v203, v64, v65
	v_cvt_pk_bf16_f32 v208, v68, v69
	v_cvt_pk_bf16_f32 v209, v72, v73
	v_cvt_pk_bf16_f32 v210, v76, v77
	v_cvt_pk_bf16_f32 v211, v80, v81
	v_sub_f32_e32 v98, v98, v2
	s_nop 0
	v_mfma_f32_32x32x16_bf16 v[114:129], v[204:207], v[200:203], v[114:129]
	v_sub_f32_e32 v99, v99, v1
	v_sub_f32_e32 v100, v100, v54
	v_sub_f32_e32 v101, v101, v55
	v_sub_f32_e32 v102, v102, v58
	v_sub_f32_e32 v103, v103, v59
	v_sub_f32_e32 v104, v104, v62
	v_sub_f32_e32 v105, v105, v63
	v_mfma_f32_32x32x16_bf16 v[114:129], v[204:207], v[208:211], v[114:129]
	v_sub_f32_e32 v106, v106, v66
	v_sub_f32_e32 v107, v107, v67
	v_sub_f32_e32 v108, v108, v70
	v_sub_f32_e32 v109, v109, v71
	v_sub_f32_e32 v110, v110, v74
	v_sub_f32_e32 v111, v111, v75
	v_sub_f32_e32 v112, v112, v78
	v_sub_f32_e32 v113, v113, v79
	s_nop 3
	v_sub_f32_e32 v114, v98, v114
	v_sub_f32_e32 v115, v99, v115
	v_sub_f32_e32 v116, v100, v116
	v_sub_f32_e32 v117, v101, v117
	v_sub_f32_e32 v118, v102, v118
	v_sub_f32_e32 v119, v103, v119
	v_sub_f32_e32 v120, v104, v120
	v_sub_f32_e32 v121, v105, v121
	v_sub_f32_e32 v122, v106, v122
	v_sub_f32_e32 v123, v107, v123
	v_sub_f32_e32 v124, v108, v124
	v_sub_f32_e32 v125, v109, v125
	v_sub_f32_e32 v126, v110, v126
	v_sub_f32_e32 v127, v111, v127
	v_sub_f32_e32 v128, v112, v128
	v_sub_f32_e32 v129, v113, v129
	v_mov_b64_e32 v[112:113], v[50:51]
	v_mov_b64_e32 v[110:111], v[48:49]
	v_mov_b64_e32 v[108:109], v[46:47]
	v_mov_b64_e32 v[106:107], v[44:45]
	v_mov_b64_e32 v[104:105], v[42:43]
	v_mov_b64_e32 v[102:103], v[40:41]
	v_mov_b64_e32 v[100:101], v[38:39]
	v_mov_b64_e32 v[98:99], v[36:37]
	v_sub_f32_e32 v37, v82, v52
	v_sub_f32_e32 v38, v83, v53
	v_mfma_f32_32x32x16_bf16 v[98:113], v[150:153], v[200:203], v[98:113]
	v_sub_f32_e32 v39, v84, v56
	v_sub_f32_e32 v40, v85, v57
	v_sub_f32_e32 v41, v86, v60
	v_sub_f32_e32 v42, v87, v61
	v_sub_f32_e32 v43, v88, v64
	v_sub_f32_e32 v44, v89, v65
	v_sub_f32_e32 v45, v90, v68
	v_mfma_f32_32x32x16_bf16 v[98:113], v[146:149], v[208:211], v[98:113]
	v_sub_f32_e32 v46, v91, v69
	v_sub_f32_e32 v47, v92, v72
	v_sub_f32_e32 v48, v93, v73
	v_sub_f32_e32 v49, v94, v76
	v_sub_f32_e32 v50, v95, v77
	v_sub_f32_e32 v51, v96, v80
	v_sub_f32_e32 v82, v97, v81
	s_mov_b32 s0, s4
	s_nop 3
	v_sub_f32_e32 v37, v37, v98
	v_sub_f32_e32 v85, v38, v99
	v_sub_f32_e32 v39, v39, v100
	v_sub_f32_e32 v40, v40, v101
	v_sub_f32_e32 v86, v41, v102
	v_sub_f32_e32 v89, v42, v103
	v_sub_f32_e32 v43, v43, v104
	v_sub_f32_e32 v44, v44, v105
	v_sub_f32_e32 v90, v45, v106
	v_sub_f32_e32 v93, v46, v107
	v_sub_f32_e32 v47, v47, v108
	v_sub_f32_e32 v48, v48, v109
	v_sub_f32_e32 v97, v49, v110
	v_sub_f32_e32 v98, v50, v111
	v_sub_f32_e32 v51, v51, v112
	v_sub_f32_e32 v99, v82, v113
	v_writelane_b32 v254, s0, 39
	v_exp_f32_e32 v84, v114
	v_exp_f32_e32 v38, v37
	v_exp_f32_e32 v83, v115
	v_exp_f32_e32 v37, v85
	v_exp_f32_e32 v88, v116
	v_exp_f32_e32 v42, v39
	v_exp_f32_e32 v87, v117
	v_exp_f32_e32 v41, v40
	v_exp_f32_e32 v92, v118
	v_exp_f32_e32 v46, v86
	v_exp_f32_e32 v91, v119
	v_exp_f32_e32 v45, v89
	v_exp_f32_e32 v96, v120
	v_exp_f32_e32 v50, v43
	v_exp_f32_e32 v95, v121
	v_exp_f32_e32 v49, v44
	v_exp_f32_e32 v86, v122
	v_exp_f32_e32 v40, v90
	v_exp_f32_e32 v85, v123
	v_exp_f32_e32 v39, v93
	v_exp_f32_e32 v90, v124
	v_exp_f32_e32 v44, v47
	v_exp_f32_e32 v89, v125
	v_exp_f32_e32 v43, v48
	v_exp_f32_e32 v94, v126
	v_exp_f32_e32 v48, v97
	v_exp_f32_e32 v93, v127
	v_exp_f32_e32 v47, v98
	v_exp_f32_e32 v98, v128
	v_exp_f32_e32 v82, v51
	v_exp_f32_e32 v97, v129
	v_exp_f32_e32 v51, v99
	v_writelane_b32 v254, s1, 40
	v_writelane_b32 v254, s2, 41
	v_writelane_b32 v254, s3, 42
	s_andn2_b64 vcc, exec, s[16:17]
	s_cbranch_vccnz .LBB0_1060
; __device__ __forceinline__ void sb_unit(int b, int h, int qb, const bf16_t* __restrict__ PROJ, bf16_t* OCAT, float* SSQO, ldsp shm, volatile LAS unsigned* FL) {
;     ...
;             if (diag) {
; #pragma unroll
;                 for (int r = 0; r < 16; ++r) { const int kk = kb0 + (r & 3) + 8 * (r >> 2); if (kk >= qabs) z0[r] = 0.f; if (kk + 32 >= qabs) z1[r] = 0.f; } }
	v_cmp_lt_i32_e64 s[92:93], v195, v163
	v_cmp_lt_i32_e64 s[94:95], v197, v163
	v_cmp_lt_i32_e64 s[90:91], v193, v163
	s_or_b64 s[92:93], s[94:95], s[92:93]
	v_cmp_lt_i32_e64 s[88:89], v191, v163
	s_or_b64 s[90:91], s[92:93], s[90:91]
	v_cmp_lt_i32_e64 s[86:87], v189, v163
	s_or_b64 s[88:89], s[90:91], s[88:89]
	v_cmp_lt_i32_e64 s[84:85], v187, v163
	s_or_b64 s[86:87], s[88:89], s[86:87]
	v_cmp_lt_i32_e64 s[82:83], v185, v163
	s_or_b64 s[84:85], s[86:87], s[84:85]
	v_cmp_lt_i32_e64 s[80:81], v183, v163
	s_or_b64 s[82:83], s[84:85], s[82:83]
	v_cmp_lt_i32_e64 s[78:79], v181, v163
	s_or_b64 s[80:81], s[82:83], s[80:81]
	v_cmp_lt_i32_e64 s[76:77], v179, v163
	s_or_b64 s[78:79], s[80:81], s[78:79]
	v_cmp_lt_i32_e64 s[74:75], v177, v163
	s_or_b64 s[76:77], s[78:79], s[76:77]
	v_cmp_lt_i32_e64 s[72:73], v175, v163
	s_or_b64 s[74:75], s[76:77], s[74:75]
	v_cmp_lt_i32_e64 s[70:71], v173, v163
	s_or_b64 s[72:73], s[74:75], s[72:73]
	v_cmp_lt_i32_e64 s[6:7], v171, v163
	s_or_b64 s[70:71], s[72:73], s[70:71]
	v_cmp_lt_i32_e64 s[4:5], v169, v163
	s_or_b64 s[6:7], s[70:71], s[6:7]
	v_cmp_lt_i32_e32 vcc, v167, v163
	s_or_b64 s[4:5], s[6:7], s[4:5]
	s_or_b64 vcc, s[4:5], vcc
	v_cmp_lt_i32_e64 s[68:69], v196, v163
	v_cndmask_b32_e32 v84, 0, v84, vcc
	v_cmp_lt_i32_e32 vcc, v166, v163
	v_cmp_lt_i32_e64 s[66:67], v194, v163
	v_cndmask_b32_e64 v83, 0, v83, s[4:5]
	s_or_b64 s[4:5], vcc, s[68:69]
	v_cmp_lt_i32_e64 s[64:65], v192, v163
	v_cndmask_b32_e64 v82, 0, v82, s[4:5]
	s_or_b64 s[4:5], s[4:5], s[66:67]
	v_cmp_lt_i32_e64 s[62:63], v190, v163
	v_cndmask_b32_e64 v47, 0, v47, s[4:5]
	s_or_b64 s[4:5], s[4:5], s[64:65]
	v_cmp_lt_i32_e64 s[60:61], v188, v163
	v_cndmask_b32_e64 v48, 0, v48, s[4:5]
	s_or_b64 s[4:5], s[4:5], s[62:63]
	v_cmp_lt_i32_e64 s[58:59], v186, v163
	v_cndmask_b32_e64 v43, 0, v43, s[4:5]
	s_or_b64 s[4:5], s[4:5], s[60:61]
	v_cmp_lt_i32_e64 s[56:57], v184, v163
	v_cndmask_b32_e64 v44, 0, v44, s[4:5]
	s_or_b64 s[4:5], s[4:5], s[58:59]
	v_cmp_lt_i32_e64 s[54:55], v182, v163
	v_cndmask_b32_e64 v39, 0, v39, s[4:5]
	s_or_b64 s[4:5], s[4:5], s[56:57]
	v_cmp_lt_i32_e64 s[52:53], v180, v163
	v_cndmask_b32_e64 v40, 0, v40, s[4:5]
	s_or_b64 s[4:5], s[4:5], s[54:55]
	v_cmp_lt_i32_e64 s[50:51], v178, v163
	v_cndmask_b32_e64 v49, 0, v49, s[4:5]
	s_or_b64 s[4:5], s[4:5], s[52:53]
	v_cmp_lt_i32_e64 s[48:49], v176, v163
	v_cndmask_b32_e64 v50, 0, v50, s[4:5]
	s_or_b64 s[4:5], s[4:5], s[50:51]
	v_cmp_lt_i32_e64 s[44:45], v174, v163
	v_cndmask_b32_e64 v45, 0, v45, s[4:5]
	s_or_b64 s[4:5], s[4:5], s[48:49]
	v_cmp_lt_i32_e64 s[42:43], v172, v163
	v_cndmask_b32_e64 v46, 0, v46, s[4:5]
	s_or_b64 s[4:5], s[4:5], s[44:45]
	v_cmp_lt_i32_e64 s[40:41], v170, v163
	v_cndmask_b32_e64 v41, 0, v41, s[4:5]
	s_or_b64 s[4:5], s[4:5], s[42:43]
	v_cmp_lt_i32_e64 s[0:1], v168, v163
	v_cndmask_b32_e64 v42, 0, v42, s[4:5]
	s_or_b64 s[4:5], s[4:5], s[40:41]
	s_or_b64 s[0:1], s[4:5], s[0:1]
	v_cndmask_b32_e64 v98, 0, v98, s[92:93]
	v_cndmask_b32_e64 v93, 0, v93, s[90:91]
	v_cndmask_b32_e64 v94, 0, v94, s[88:89]
	v_cndmask_b32_e64 v89, 0, v89, s[86:87]
	v_cndmask_b32_e64 v90, 0, v90, s[84:85]
	v_cndmask_b32_e64 v85, 0, v85, s[82:83]
	v_cndmask_b32_e64 v86, 0, v86, s[80:81]
	v_cndmask_b32_e64 v95, 0, v95, s[78:79]
	v_cndmask_b32_e64 v96, 0, v96, s[76:77]
	v_cndmask_b32_e64 v91, 0, v91, s[74:75]
	v_cndmask_b32_e64 v92, 0, v92, s[72:73]
	v_cndmask_b32_e64 v87, 0, v87, s[70:71]
	v_cndmask_b32_e64 v88, 0, v88, s[6:7]
	v_cndmask_b32_e64 v97, 0, v97, s[94:95]
	v_cndmask_b32_e64 v37, 0, v37, s[4:5]
	v_cndmask_b32_e64 v38, 0, v38, s[0:1]
	v_cndmask_b32_e32 v51, 0, v51, vcc
